# pipelined attention + barrier every tile with LDS fragment prefetch running across the barrier (no post-barrier bubble)
# baseline (speedup 1.0000x reference)
.LBB0_733:
	s_or_b64 exec, exec, s[8:9]
	s_movk_i32 s4, 0xf0
	s_cmp_lg_u32 0, -1
	v_lshlrev_b32_e32 v39, 8, v141
	v_bitop3_b32 v80, v142, s4, v136 bitop3:0x48
	s_cselect_b32 s10, 0, 0
	v_cvt_pk_bf16_f32 v96, v134, v135
	v_cvt_pk_bf16_f32 v97, v132, v133
	v_cvt_pk_bf16_f32 v98, v130, v131
	v_cvt_pk_bf16_f32 v99, v128, v129
	v_cvt_pk_bf16_f32 v100, v126, v127
	v_cvt_pk_bf16_f32 v101, v124, v125
	v_cvt_pk_bf16_f32 v102, v122, v123
	v_cvt_pk_bf16_f32 v103, v120, v121
	v_cvt_pk_bf16_f32 v104, v70, v71
	v_cvt_pk_bf16_f32 v105, v74, v75
	v_cvt_pk_bf16_f32 v106, v64, v65
	v_cvt_pk_bf16_f32 v107, v68, v69
	v_cvt_pk_bf16_f32 v108, v60, v61
	v_cvt_pk_bf16_f32 v109, v66, v67
	v_cvt_pk_bf16_f32 v110, v56, v57
	v_cvt_pk_bf16_f32 v111, v58, v59
	v_cvt_pk_bf16_f32 v112, v112, v113
	v_cvt_pk_bf16_f32 v113, v118, v119
	v_cvt_pk_bf16_f32 v114, v114, v115
	v_cvt_pk_bf16_f32 v115, v116, v117
	v_cvt_pk_bf16_f32 v116, v78, v79
	v_cvt_pk_bf16_f32 v117, v76, v77
	v_cvt_pk_bf16_f32 v118, v72, v73
	v_cvt_pk_bf16_f32 v119, v62, v63
	v_cvt_pk_bf16_f32 v120, v52, v53
	v_cvt_pk_bf16_f32 v121, v54, v55
	v_cvt_pk_bf16_f32 v122, v46, v47
	v_cvt_pk_bf16_f32 v123, v50, v51
	v_cvt_pk_bf16_f32 v124, v44, v45
	v_cvt_pk_bf16_f32 v125, v48, v49
	v_cvt_pk_bf16_f32 v126, v40, v41
	v_cvt_pk_bf16_f32 v127, v42, v43
	v_readlane_b32 s100, v250, 8
	v_mbcnt_lo_u32_b32 v68, -1, 0
	v_mbcnt_hi_u32_b32 v68, -1, v68
	s_nop 1
	v_add_u32_e32 v69, s100, v68
	v_lshrrev_b32_e32 v70, 3, v69
	v_and_b32_e32 v71, 7, v69
	v_lshrrev_b32_e32 v72, 2, v71
	v_bfe_u32 v73, v71, 1, 1
	v_and_b32_e32 v74, 1, v71
	v_lshlrev_b32_e32 v74, 1, v74
	v_lshl_add_u32 v75, v72, 2, v74
	v_bfe_u32 v76, v70, 1, 3
	v_xor_b32_e32 v77, v75, v76
	v_add_u32_e32 v78, 1, v75
	v_xor_b32_e32 v78, v78, v76
	v_lshlrev_b32_e32 v79, 7, v70
	v_lshl_add_u32 v79, v73, 3, v79
	v_lshl_add_u32 v64, v77, 4, v79
	v_lshl_add_u32 v65, v78, 4, v79
	v_add_u32_e32 v66, 0x2000, v64
	v_add_u32_e32 v67, 0x2000, v65
	v_or_b32_e32 v81, v39, v80
	s_add_i32 s15, s10, 0x10000
	v_and_b32_e32 v82, 6, v137
	v_lshrrev_b32_e32 v84, 4, v136
	s_waitcnt vmcnt(0)
	s_waitcnt vmcnt(0)
	s_add_i32 s11, s10, 0x12000
	v_lshl_add_u32 v83, v139, 7, s10
	v_bitop3_b32 v85, v84, v82, 7 bitop3:0x6c
	v_and_b32_e32 v86, 8, v138
	v_or_b32_e32 v82, 1, v82
	v_add_u32_e32 v225, s15, v81
	s_waitcnt vmcnt(4)
	ds_write_b128 v225, v[24:27] offset:0
	v_lshlrev_b32_e32 v85, 4, v85
	v_add_u32_e32 v87, v83, v86
	v_bitop3_b32 v82, v84, v82, 7 bitop3:0x6c
	v_add3_u32 v226, v80, s11, v39
	ds_write_b128 v226, v[28:31] offset:0
	v_lshlrev_b32_e32 v82, 4, v82
	v_add_u32_e32 v227, v87, v85
	ds_write_b64 v64, v[12:13] offset:0
	v_lshrrev_b32_e32 v32, 5, v136
	v_add_u32_e32 v83, 0x2000, v83
	v_or_b32_e32 v84, v85, v86
	v_add_u32_e32 v228, v87, v82
	ds_write_b64 v65, v[14:15] offset:0
	v_xor_b32_e32 v32, v32, v137
	v_or_b32_e32 v86, v82, v86
	v_add_u32_e32 v229, v84, v83
	ds_write_b64 v66, v[4:5] offset:0
	v_lshlrev_b32_e32 v32, 4, v32
	v_add_u32_e32 v184, v86, v83
	ds_write_b64 v67, v[6:7] offset:0
	v_lshlrev_b32_e32 v33, 8, v143
	v_and_b32_e32 v32, 16, v32
	v_bfe_u32 v35, v137, 1, 3
	s_waitcnt vmcnt(4)
	ds_write_b128 v225, v[20:23] offset:0x4000
	v_lshlrev_b32_e32 v36, 5, v35
	v_add3_u32 v32, v33, s15, v32
	s_movk_i32 s16, 0x60
	ds_write_b128 v226, v[16:19] offset:0x4000
	v_xad_u32 v204, v36, s16, v32
	s_movk_i32 s16, 0x80
	ds_write_b64 v64, v[8:9] offset:0x4000
	v_xad_u32 v205, v36, s16, v32
	s_movk_i32 s16, 0xa0
	ds_write_b64 v65, v[10:11] offset:0x4000
	s_add_u32 s8, s6, 0x100
	v_xad_u32 v206, v36, s16, v32
	s_movk_i32 s16, 0xc0
	ds_write_b64 v66, v[0:1] offset:0x4000
	s_addc_u32 s9, s7, 0
	v_xad_u32 v207, v36, s16, v32
	s_movk_i32 s16, 0xe0
	ds_write_b64 v67, v[2:3] offset:0x4000
	v_add_u32_e32 v201, v32, v36
	v_xad_u32 v202, v36, 32, v32
	v_xad_u32 v203, v36, 64, v32
	v_xad_u32 v208, v36, s16, v32
	v_lshl_add_u32 v32, v143, 7, s10
	s_add_u32 s10, s78, 0x20000
	global_load_dwordx4 v[132:135], v198, s[8:9]
	s_addc_u32 s11, s79, 0
	global_load_dwordx4 v[128:131], v199, s[8:9]
	v_lshrrev_b32_e32 v34, 1, v137
	global_load_dwordx4 v[136:139], v196, s[10:11]
	s_add_u32 s6, s6, 0x180
	v_bitop3_b32 v34, v140, v34, 7 bitop3:0x78
	v_bitop3_b32 v37, v140, v35, 2 bitop3:0x36
	v_bitop3_b32 v38, v140, v35, 4 bitop3:0x36
	v_bitop3_b32 v35, v140, v35, 6 bitop3:0x36
	global_load_dwordx4 v[140:143], v197, s[10:11]
	s_addc_u32 s7, s7, 0
	s_add_u32 s8, s78, 0x30000
	global_load_dwordx4 v[148:151], v198, s[6:7]
	s_addc_u32 s9, s79, 0
	global_load_dwordx4 v[144:147], v199, s[6:7]
	global_load_dwordx4 v[152:155], v196, s[8:9]
	s_add_u32 s10, s13, s14
	global_load_dwordx4 v[156:159], v197, s[8:9]
	s_addc_u32 s11, s12, 0
	s_add_u32 s12, s41, s30
	v_mov_b32_e32 v0, 0
	s_mov_b32 s4, 0
	v_lshl_add_u32 v209, v34, 4, v32
	v_lshl_add_u32 v210, v37, 4, v32
	v_lshl_add_u32 v211, v38, 4, v32
	v_lshl_add_u32 v224, v35, 4, v32
	s_addc_u32 s13, 0, s31
	v_mov_b32_e32 v1, v0
	v_mov_b32_e32 v2, v0
	v_mov_b32_e32 v3, v0
	v_mov_b32_e32 v4, v0
	v_mov_b32_e32 v5, v0
	v_mov_b32_e32 v6, v0
	v_mov_b32_e32 v7, v0
	v_mov_b32_e32 v8, v0
	v_mov_b32_e32 v9, v0
	v_mov_b32_e32 v10, v0
	v_mov_b32_e32 v11, v0
	v_mov_b32_e32 v12, v0
	v_mov_b32_e32 v13, v0
	v_mov_b32_e32 v14, v0
	v_mov_b32_e32 v15, v0
	v_mov_b32_e32 v16, v0
	v_mov_b32_e32 v17, v0
	v_mov_b32_e32 v18, v0
	v_mov_b32_e32 v19, v0
	v_mov_b32_e32 v20, v0
	v_mov_b32_e32 v21, v0
	v_mov_b32_e32 v22, v0
	v_mov_b32_e32 v23, v0
	v_mov_b32_e32 v24, v0
	v_mov_b32_e32 v25, v0
	v_mov_b32_e32 v26, v0
	v_mov_b32_e32 v27, v0
	v_mov_b32_e32 v28, v0
	v_mov_b32_e32 v29, v0
	v_mov_b32_e32 v30, v0
	v_mov_b32_e32 v31, v0
	v_mov_b32_e32 v32, v0
	v_mov_b32_e32 v33, v0
	v_mov_b32_e32 v34, v0
	v_mov_b32_e32 v35, v0
	v_mov_b32_e32 v36, v0
	v_mov_b32_e32 v37, v0
	v_mov_b32_e32 v38, v0
	v_mov_b32_e32 v39, v0
	v_mov_b32_e32 v40, v0
	v_mov_b32_e32 v41, v0
	v_mov_b32_e32 v42, v0
	v_mov_b32_e32 v43, v0
	v_mov_b32_e32 v44, v0
	v_mov_b32_e32 v45, v0
	v_mov_b32_e32 v46, v0
	v_mov_b32_e32 v47, v0
	v_mov_b32_e32 v48, v0
	v_mov_b32_e32 v49, v0
	v_mov_b32_e32 v50, v0
	v_mov_b32_e32 v51, v0
	v_mov_b32_e32 v52, v0
	v_mov_b32_e32 v53, v0
	v_mov_b32_e32 v54, v0
	v_mov_b32_e32 v55, v0
	v_mov_b32_e32 v56, v0
	v_mov_b32_e32 v57, v0
	v_mov_b32_e32 v58, v0
	v_mov_b32_e32 v59, v0
	v_mov_b32_e32 v60, v0
	v_mov_b32_e32 v61, v0
	v_mov_b32_e32 v62, v0
	v_mov_b32_e32 v63, v0
	v_mov_b32_e32 v160, v0
	v_mov_b32_e32 v161, v0
	v_mov_b32_e32 v227, v64
	v_mov_b32_e32 v228, v65
	v_mov_b32_e32 v229, v66
	v_mov_b32_e32 v184, v67
	v_readlane_b32 s100, v250, 8
	v_mbcnt_lo_u32_b32 v68, -1, 0
	v_mbcnt_hi_u32_b32 v68, -1, v68
	v_and_b32_e32 v69, 15, v68
	v_lshrrev_b32_e32 v70, 4, v68
	v_lshlrev_b32_e32 v72, 8, v69
	v_add_u32_e32 v72, 0x10000, v72
	v_add_u32_e32 v71, 0, v70
	v_xor_b32_e32 v71, v71, v69
	v_lshl_add_u32 v201, v71, 4, v72
	v_add_u32_e32 v71, 4, v70
	v_xor_b32_e32 v71, v71, v69
	v_lshl_add_u32 v202, v71, 4, v72
	v_add_u32_e32 v71, 8, v70
	v_xor_b32_e32 v71, v71, v69
	v_lshl_add_u32 v203, v71, 4, v72
	v_add_u32_e32 v71, 12, v70
	v_xor_b32_e32 v71, v71, v69
	v_lshl_add_u32 v246, v71, 4, v72
	v_bfe_u32 v73, v69, 1, 3
	v_lshlrev_b32_e32 v76, 7, v69
	v_add_u32_e32 v71, 0, v70
	v_xor_b32_e32 v71, v71, v73
	v_lshl_add_u32 v209, v71, 4, v76
	v_add_u32_e32 v71, 4, v70
	v_xor_b32_e32 v71, v71, v73
	v_lshl_add_u32 v210, v71, 4, v76
	s_lshl_b32 s101, s100, 7
	s_add_u32 s101, s101, 0x8000
	s_cmpk_ge_u32 s100, 0x100
	s_cselect_b32 s6, 0x8000, 0
	s_add_u32 s101, s101, s6
	v_and_b32_e32 v74, 31, v68
	v_lshrrev_b32_e32 v75, 5, v68
	v_lshlrev_b32_e32 v74, 8, v74
	v_lshl_add_u32 v74, v75, 4, v74
	v_add_u32_e32 v74, s101, v74
	v_lshlrev_b32_e32 v75, 8, v69
	v_lshl_add_u32 v75, v70, 4, v75
	v_add_u32_e32 v75, s101, v75
	ds_write_b128 v74, v[96:99] offset:0
	ds_write_b128 v74, v[100:103] offset:32
	ds_write_b128 v74, v[104:107] offset:64
	ds_write_b128 v74, v[108:111] offset:96
	ds_write_b128 v74, v[112:115] offset:128
	ds_write_b128 v74, v[116:119] offset:160
	ds_write_b128 v74, v[120:123] offset:192
	ds_write_b128 v74, v[124:127] offset:224
	s_waitcnt lgkmcnt(0)
	ds_read_b128 v[96:99], v75 offset:0
	ds_read_b128 v[100:103], v75 offset:64
	ds_read_b128 v[104:107], v75 offset:128
	ds_read_b128 v[108:111], v75 offset:192
	ds_read_b128 v[112:115], v75 offset:4096
	ds_read_b128 v[116:119], v75 offset:4160
	ds_read_b128 v[120:123], v75 offset:4224
	ds_read_b128 v[124:127], v75 offset:4288
	s_waitcnt vmcnt(0)
	s_waitcnt lgkmcnt(0)
	s_barrier
	ds_write_b128 v225, v[136:139] offset:32768
	ds_write_b128 v226, v[140:143] offset:32768
	s_add_u32 s15, s22, s12
	s_addc_u32 s14, s23, s13
	s_add_u32 s6, s15, 0x23a40000
	s_addc_u32 s7, s14, 0
	s_waitcnt lgkmcnt(0)
	global_load_dwordx4 v[136:139], v196, s[6:7]
	global_load_dwordx4 v[140:143], v197, s[6:7]
	v_mov_b32_e32 v194, 0
	v_mov_b32_e32 v195, 0
	s_barrier
	ds_read_b128 v[160:163], v201 offset:0
	ds_read_b128 v[164:167], v202 offset:0
	ds_read_b128 v[168:171], v203 offset:0
	ds_read_b128 v[172:175], v246 offset:0
	ds_read_b128 v[176:179], v201 offset:4096
	ds_read_b128 v[180:183], v202 offset:4096
	ds_read_b128 v[230:233], v203 offset:4096
	s_waitcnt lgkmcnt(6)
	v_mfma_f32_16x16x32_bf16 v[64:67], v[160:163], v[96:99], 0
	v_mfma_f32_16x16x32_bf16 v[68:71], v[160:163], v[112:115], 0
	ds_read_b128 v[234:237], v246 offset:4096
	s_waitcnt lgkmcnt(6)
	v_mfma_f32_16x16x32_bf16 v[68:71], v[164:167], v[116:119], v[68:71]
	v_mfma_f32_16x16x32_bf16 v[64:67], v[164:167], v[100:103], v[64:67]
	ds_read_b128 v[160:163], v201 offset:8192
	s_waitcnt lgkmcnt(6)
	v_mfma_f32_16x16x32_bf16 v[64:67], v[168:171], v[104:107], v[64:67]
	v_mfma_f32_16x16x32_bf16 v[68:71], v[168:171], v[120:123], v[68:71]
	ds_read_b128 v[164:167], v202 offset:8192
	s_waitcnt lgkmcnt(6)
	v_mfma_f32_16x16x32_bf16 v[68:71], v[172:175], v[124:127], v[68:71]
	v_mfma_f32_16x16x32_bf16 v[64:67], v[172:175], v[108:111], v[64:67]
	ds_read_b128 v[168:171], v203 offset:8192
	s_waitcnt lgkmcnt(6)
	v_mfma_f32_16x16x32_bf16 v[72:75], v[176:179], v[96:99], 0
	s_nop 7
	s_nop 1
	v_exp_f32_e32 v64, v64
	v_exp_f32_e32 v68, v68
	v_mfma_f32_16x16x32_bf16 v[76:79], v[176:179], v[112:115], 0
	v_exp_f32_e32 v65, v65
	v_exp_f32_e32 v69, v69
	ds_read_b128 v[172:175], v246 offset:8192
	s_waitcnt lgkmcnt(6)
	v_mfma_f32_16x16x32_bf16 v[76:79], v[180:183], v[116:119], v[76:79]
	v_exp_f32_e32 v66, v66
	v_exp_f32_e32 v70, v70
	v_mfma_f32_16x16x32_bf16 v[72:75], v[180:183], v[100:103], v[72:75]
	v_exp_f32_e32 v67, v67
	v_exp_f32_e32 v71, v71
	ds_read_b128 v[176:179], v201 offset:12288
	s_waitcnt lgkmcnt(6)
	v_mfma_f32_16x16x32_bf16 v[72:75], v[230:233], v[104:107], v[72:75]
	v_add_f32_e32 v220, v64, v65
	v_add_f32_e32 v221, v68, v69
	v_mfma_f32_16x16x32_bf16 v[76:79], v[230:233], v[120:123], v[76:79]
	v_add_f32_e32 v220, v220, v66
	v_add_f32_e32 v221, v221, v70
	ds_read_b128 v[180:183], v202 offset:12288
	s_waitcnt lgkmcnt(6)
	v_mfma_f32_16x16x32_bf16 v[76:79], v[234:237], v[124:127], v[76:79]
	v_add_f32_e32 v220, v220, v67
	v_mfma_f32_16x16x32_bf16 v[72:75], v[234:237], v[108:111], v[72:75]
	v_add_f32_e32 v221, v221, v71
	ds_read_b128 v[230:233], v203 offset:12288
	s_waitcnt lgkmcnt(6)
	v_mfma_f32_16x16x32_bf16 v[80:83], v[160:163], v[96:99], 0
	s_nop 7
	s_nop 1
	v_exp_f32_e32 v72, v72
	v_exp_f32_e32 v76, v76
	v_exp_f32_e32 v73, v73
	v_mfma_f32_16x16x32_bf16 v[84:87], v[160:163], v[112:115], 0
	v_exp_f32_e32 v77, v77
	v_exp_f32_e32 v74, v74
	v_exp_f32_e32 v78, v78
	ds_read_b128 v[234:237], v246 offset:12288
	s_waitcnt lgkmcnt(6)
	v_mfma_f32_16x16x32_bf16 v[84:87], v[164:167], v[116:119], v[84:87]
	v_exp_f32_e32 v75, v75
	v_exp_f32_e32 v79, v79
	v_add_f32_e32 v220, v220, v72
	v_mfma_f32_16x16x32_bf16 v[80:83], v[164:167], v[100:103], v[80:83]
	v_add_f32_e32 v221, v221, v76
	v_add_f32_e32 v220, v220, v73
	v_add_f32_e32 v221, v221, v77
	ds_read_b128 v[160:163], v201 offset:16384
	s_waitcnt lgkmcnt(6)
	v_mfma_f32_16x16x32_bf16 v[80:83], v[168:171], v[104:107], v[80:83]
	v_add_f32_e32 v220, v220, v74
	v_add_f32_e32 v221, v221, v78
	v_add_f32_e32 v220, v220, v75
	v_mfma_f32_16x16x32_bf16 v[84:87], v[168:171], v[120:123], v[84:87]
	v_add_f32_e32 v221, v221, v79
	v_cvt_pk_bf16_f32 v216, v64, v65
	v_cvt_pk_bf16_f32 v217, v66, v67
	ds_read_b128 v[164:167], v209 offset:0
	s_waitcnt lgkmcnt(6)
	v_mfma_f32_16x16x32_bf16 v[84:87], v[172:175], v[124:127], v[84:87]
	v_cvt_pk_bf16_f32 v238, v68, v69
	v_cvt_pk_bf16_f32 v239, v70, v71
	v_cvt_pk_bf16_f32 v218, v72, v73
	v_mfma_f32_16x16x32_bf16 v[80:83], v[172:175], v[108:111], v[80:83]
	v_cvt_pk_bf16_f32 v219, v74, v75
	v_cvt_pk_bf16_f32 v240, v76, v77
	v_cvt_pk_bf16_f32 v241, v78, v79
	ds_read_b128 v[168:171], v202 offset:16384
	s_waitcnt lgkmcnt(6)
	v_mfma_f32_16x16x32_bf16 v[88:91], v[176:179], v[96:99], 0
	s_nop 7
	s_nop 1
	v_exp_f32_e32 v80, v80
	v_exp_f32_e32 v84, v84
	v_mfma_f32_16x16x32_bf16 v[92:95], v[176:179], v[112:115], 0
	v_exp_f32_e32 v81, v81
	v_exp_f32_e32 v85, v85
	ds_read_b128 v[172:175], v209 offset:2048
	s_waitcnt lgkmcnt(6)
	v_mfma_f32_16x16x32_bf16 v[92:95], v[180:183], v[116:119], v[92:95]
	v_exp_f32_e32 v82, v82
	v_exp_f32_e32 v86, v86
	v_mfma_f32_16x16x32_bf16 v[88:91], v[180:183], v[100:103], v[88:91]
	v_exp_f32_e32 v83, v83
	v_exp_f32_e32 v87, v87
	ds_read_b128 v[176:179], v203 offset:16384
	s_waitcnt lgkmcnt(6)
	v_mfma_f32_16x16x32_bf16 v[88:91], v[230:233], v[104:107], v[88:91]
	v_add_f32_e32 v220, v220, v80
	v_add_f32_e32 v221, v221, v84
	v_mfma_f32_16x16x32_bf16 v[92:95], v[230:233], v[120:123], v[92:95]
	v_add_f32_e32 v220, v220, v81
	v_add_f32_e32 v221, v221, v85
	ds_read_b128 v[180:183], v209 offset:4096
	s_waitcnt lgkmcnt(6)
	v_mfma_f32_16x16x32_bf16 v[92:95], v[234:237], v[124:127], v[92:95]
	v_add_f32_e32 v220, v220, v82
	v_add_f32_e32 v221, v221, v86
	v_mfma_f32_16x16x32_bf16 v[88:91], v[234:237], v[108:111], v[88:91]
	v_add_f32_e32 v220, v220, v83
	v_add_f32_e32 v221, v221, v87
	ds_read_b128 v[230:233], v246 offset:16384
	s_nop 7
.LBB0_734:
	s_waitcnt lgkmcnt(6)
	v_mfma_f32_16x16x32_bf16 v[64:67], v[160:163], v[96:99], 0
	v_exp_f32_e32 v88, v88
	v_exp_f32_e32 v92, v92
	v_mfma_f32_16x16x32_bf16 v[68:71], v[160:163], v[112:115], 0
	v_cvt_pk_bf16_f32 v242, v80, v81
	v_exp_f32_e32 v89, v89
	ds_read_b128 v[234:237], v209 offset:6144
	s_add_u32 s16, s22, s10
	s_addc_u32 s17, s23, s11
	s_add_u32 s15, s22, s12
	s_addc_u32 s14, s23, s13
	s_add_u32 s8, s16, 0x3bc00200
	s_addc_u32 s9, s17, 0
	s_add_u32 s6, s15, 0x23a50000
	s_addc_u32 s7, s14, 0
	s_waitcnt lgkmcnt(6)
	v_mfma_f32_16x16x32_bf16 v[0:3], v[164:167], v[216:219], v[0:3]
	v_exp_f32_e32 v93, v93
	v_cvt_pk_bf16_f32 v243, v82, v83
	v_mfma_f32_16x16x32_bf16 v[4:7], v[164:167], v[238:241], v[4:7]
	v_exp_f32_e32 v90, v90
	v_exp_f32_e32 v94, v94
	ds_read_b128 v[160:163], v201 offset:20480
	s_waitcnt vmcnt(4)
	ds_write_b128 v225, v[152:155] offset:49152
	s_waitcnt lgkmcnt(7)
	v_mfma_f32_16x16x32_bf16 v[68:71], v[168:171], v[116:119], v[68:71]
	v_cvt_pk_bf16_f32 v204, v84, v85
	v_mfma_f32_16x16x32_bf16 v[64:67], v[168:171], v[100:103], v[64:67]
	v_exp_f32_e32 v91, v91
	ds_read_b128 v[164:167], v209 offset:8192
	ds_write_b128 v226, v[156:159] offset:49152
	s_waitcnt lgkmcnt(8)
	v_mfma_f32_16x16x32_bf16 v[12:15], v[172:175], v[238:241], v[12:15]
	v_exp_f32_e32 v95, v95
	v_mfma_f32_16x16x32_bf16 v[8:11], v[172:175], v[216:219], v[8:11]
	v_cvt_pk_bf16_f32 v205, v86, v87
	ds_read_b128 v[168:171], v202 offset:20480
	ds_write_b64 v227, v[132:133] offset:32768
	s_waitcnt lgkmcnt(9)
	v_mfma_f32_16x16x32_bf16 v[64:67], v[176:179], v[104:107], v[64:67]
	v_add_f32_e32 v220, v220, v88
	v_mfma_f32_16x16x32_bf16 v[68:71], v[176:179], v[120:123], v[68:71]
	v_add_f32_e32 v221, v221, v92
	ds_read_b128 v[172:175], v209 offset:10240
	ds_write_b64 v228, v[134:135] offset:32768
	s_waitcnt lgkmcnt(10)
	v_mfma_f32_16x16x32_bf16 v[16:19], v[180:183], v[216:219], v[16:19]
	v_add_f32_e32 v220, v220, v89
	v_mfma_f32_16x16x32_bf16 v[20:23], v[180:183], v[238:241], v[20:23]
	v_add_f32_e32 v221, v221, v93
	ds_read_b128 v[176:179], v203 offset:20480
	ds_write_b64 v229, v[128:129] offset:32768
	s_waitcnt lgkmcnt(11)
	v_mfma_f32_16x16x32_bf16 v[68:71], v[230:233], v[124:127], v[68:71]
	v_cvt_pk_bf16_f32 v244, v88, v89
	v_mfma_f32_16x16x32_bf16 v[64:67], v[230:233], v[108:111], v[64:67]
	v_cvt_pk_bf16_f32 v245, v90, v91
	ds_read_b128 v[180:183], v209 offset:12288
	ds_write_b64 v184, v[130:131] offset:32768
	s_waitcnt lgkmcnt(12)
	v_mfma_f32_16x16x32_bf16 v[28:31], v[234:237], v[238:241], v[28:31]
	v_cvt_pk_bf16_f32 v206, v92, v93
	v_mfma_f32_16x16x32_bf16 v[24:27], v[234:237], v[216:219], v[24:27]
	v_cvt_pk_bf16_f32 v207, v94, v95
	ds_read_b128 v[230:233], v246 offset:20480
	global_load_dwordx4 v[132:135], v198, s[8:9]
	s_waitcnt lgkmcnt(12)
	v_mfma_f32_16x16x32_bf16 v[72:75], v[160:163], v[96:99], 0
	v_add_f32_e32 v220, v220, v90
	v_add_f32_e32 v221, v221, v94
	v_mfma_f32_16x16x32_bf16 v[76:79], v[160:163], v[112:115], 0
	v_add_f32_e32 v220, v220, v91
	v_add_f32_e32 v221, v221, v95
	ds_read_b128 v[234:237], v209 offset:14336
	global_load_dwordx4 v[128:131], v199, s[8:9]
	s_waitcnt lgkmcnt(11)
	v_mfma_f32_16x16x32_bf16 v[32:35], v[164:167], v[216:219], v[32:35]
	v_add_f32_e32 v194, v194, v220
	v_add_f32_e32 v195, v195, v221
	v_mfma_f32_16x16x32_bf16 v[36:39], v[164:167], v[238:241], v[36:39]
	v_exp_f32_e32 v64, v64
	v_exp_f32_e32 v68, v68
	ds_read_b128 v[160:163], v201 offset:24576
	global_load_dwordx4 v[152:155], v196, s[6:7]
	s_waitcnt lgkmcnt(10)
	v_mfma_f32_16x16x32_bf16 v[76:79], v[168:171], v[116:119], v[76:79]
	v_exp_f32_e32 v65, v65
	v_mfma_f32_16x16x32_bf16 v[72:75], v[168:171], v[100:103], v[72:75]
	v_exp_f32_e32 v69, v69
	ds_read_b128 v[164:167], v210 offset:0
	global_load_dwordx4 v[156:159], v197, s[6:7]
	s_waitcnt lgkmcnt(9)
	v_mfma_f32_16x16x32_bf16 v[44:47], v[172:175], v[238:241], v[44:47]
	v_exp_f32_e32 v66, v66
	v_mfma_f32_16x16x32_bf16 v[40:43], v[172:175], v[216:219], v[40:43]
	v_exp_f32_e32 v70, v70
	ds_read_b128 v[168:171], v202 offset:24576
	s_waitcnt lgkmcnt(8)
	v_mfma_f32_16x16x32_bf16 v[72:75], v[176:179], v[104:107], v[72:75]
	v_exp_f32_e32 v67, v67
	v_mfma_f32_16x16x32_bf16 v[76:79], v[176:179], v[120:123], v[76:79]
	v_exp_f32_e32 v71, v71
	ds_read_b128 v[172:175], v210 offset:2048
	s_waitcnt lgkmcnt(7)
	v_mfma_f32_16x16x32_bf16 v[48:51], v[180:183], v[216:219], v[48:51]
	v_add_f32_e32 v220, v64, v65
	v_mfma_f32_16x16x32_bf16 v[52:55], v[180:183], v[238:241], v[52:55]
	v_add_f32_e32 v221, v68, v69
	ds_read_b128 v[176:179], v203 offset:24576
	s_waitcnt lgkmcnt(6)
	v_mfma_f32_16x16x32_bf16 v[76:79], v[230:233], v[124:127], v[76:79]
	v_add_f32_e32 v220, v220, v66
	v_mfma_f32_16x16x32_bf16 v[72:75], v[230:233], v[108:111], v[72:75]
	v_add_f32_e32 v221, v221, v70
	ds_read_b128 v[180:183], v210 offset:4096
	s_waitcnt lgkmcnt(6)
	v_mfma_f32_16x16x32_bf16 v[60:63], v[234:237], v[238:241], v[60:63]
	v_add_f32_e32 v220, v220, v67
	v_mfma_f32_16x16x32_bf16 v[56:59], v[234:237], v[216:219], v[56:59]
	v_add_f32_e32 v221, v221, v71
	ds_read_b128 v[230:233], v246 offset:24576
	s_waitcnt lgkmcnt(6)
	v_mfma_f32_16x16x32_bf16 v[80:83], v[160:163], v[96:99], 0
	v_exp_f32_e32 v72, v72
	v_exp_f32_e32 v76, v76
	v_mfma_f32_16x16x32_bf16 v[84:87], v[160:163], v[112:115], 0
	v_exp_f32_e32 v73, v73
	v_exp_f32_e32 v77, v77
	ds_read_b128 v[234:237], v210 offset:6144
	s_waitcnt lgkmcnt(6)
	v_mfma_f32_16x16x32_bf16 v[0:3], v[164:167], v[242:245], v[0:3]
	v_exp_f32_e32 v74, v74
	v_exp_f32_e32 v78, v78
	v_mfma_f32_16x16x32_bf16 v[4:7], v[164:167], v[204:207], v[4:7]
	v_exp_f32_e32 v75, v75
	v_exp_f32_e32 v79, v79
	ds_read_b128 v[160:163], v201 offset:28672
	s_waitcnt lgkmcnt(6)
	v_mfma_f32_16x16x32_bf16 v[84:87], v[168:171], v[116:119], v[84:87]
	v_add_f32_e32 v220, v220, v72
	v_mfma_f32_16x16x32_bf16 v[80:83], v[168:171], v[100:103], v[80:83]
	v_add_f32_e32 v221, v221, v76
	ds_read_b128 v[164:167], v210 offset:8192
	s_waitcnt lgkmcnt(6)
	v_mfma_f32_16x16x32_bf16 v[12:15], v[172:175], v[204:207], v[12:15]
	v_add_f32_e32 v220, v220, v73
	v_mfma_f32_16x16x32_bf16 v[8:11], v[172:175], v[242:245], v[8:11]
	v_add_f32_e32 v221, v221, v77
	ds_read_b128 v[168:171], v202 offset:28672
	s_waitcnt lgkmcnt(6)
	v_mfma_f32_16x16x32_bf16 v[80:83], v[176:179], v[104:107], v[80:83]
	v_add_f32_e32 v220, v220, v74
	v_mfma_f32_16x16x32_bf16 v[84:87], v[176:179], v[120:123], v[84:87]
	v_add_f32_e32 v221, v221, v78
	ds_read_b128 v[172:175], v210 offset:10240
	s_waitcnt lgkmcnt(6)
	v_mfma_f32_16x16x32_bf16 v[16:19], v[180:183], v[242:245], v[16:19]
	v_add_f32_e32 v220, v220, v75
	v_mfma_f32_16x16x32_bf16 v[20:23], v[180:183], v[204:207], v[20:23]
	v_add_f32_e32 v221, v221, v79
	ds_read_b128 v[176:179], v203 offset:28672
	s_waitcnt lgkmcnt(6)
	v_mfma_f32_16x16x32_bf16 v[84:87], v[230:233], v[124:127], v[84:87]
	v_cvt_pk_bf16_f32 v216, v64, v65
	v_mfma_f32_16x16x32_bf16 v[80:83], v[230:233], v[108:111], v[80:83]
	v_cvt_pk_bf16_f32 v217, v66, v67
	ds_read_b128 v[180:183], v210 offset:12288
	s_waitcnt lgkmcnt(6)
	v_mfma_f32_16x16x32_bf16 v[28:31], v[234:237], v[204:207], v[28:31]
	v_cvt_pk_bf16_f32 v238, v68, v69
	v_mfma_f32_16x16x32_bf16 v[24:27], v[234:237], v[242:245], v[24:27]
	v_cvt_pk_bf16_f32 v239, v70, v71
	ds_read_b128 v[230:233], v246 offset:28672
	s_waitcnt lgkmcnt(6)
	v_mfma_f32_16x16x32_bf16 v[88:91], v[160:163], v[96:99], 0
	v_exp_f32_e32 v80, v80
	v_exp_f32_e32 v84, v84
	v_mfma_f32_16x16x32_bf16 v[92:95], v[160:163], v[112:115], 0
	v_exp_f32_e32 v81, v81
	v_exp_f32_e32 v85, v85
	ds_read_b128 v[234:237], v210 offset:14336
	s_waitcnt lgkmcnt(6)
	v_mfma_f32_16x16x32_bf16 v[32:35], v[164:167], v[242:245], v[32:35]
	v_exp_f32_e32 v82, v82
	v_exp_f32_e32 v86, v86
	v_mfma_f32_16x16x32_bf16 v[36:39], v[164:167], v[204:207], v[36:39]
	v_exp_f32_e32 v83, v83
	v_exp_f32_e32 v87, v87
	ds_read_b128 v[160:163], v201 offset:32768
	s_waitcnt lgkmcnt(6)
	v_mfma_f32_16x16x32_bf16 v[92:95], v[168:171], v[116:119], v[92:95]
	v_add_f32_e32 v220, v220, v80
	v_mfma_f32_16x16x32_bf16 v[88:91], v[168:171], v[100:103], v[88:91]
	v_add_f32_e32 v221, v221, v84
	ds_read_b128 v[164:167], v209 offset:16384
	s_waitcnt lgkmcnt(6)
	v_mfma_f32_16x16x32_bf16 v[44:47], v[172:175], v[204:207], v[44:47]
	v_add_f32_e32 v220, v220, v81
	v_mfma_f32_16x16x32_bf16 v[40:43], v[172:175], v[242:245], v[40:43]
	v_add_f32_e32 v221, v221, v85
	ds_read_b128 v[168:171], v202 offset:32768
	s_waitcnt lgkmcnt(6)
	v_mfma_f32_16x16x32_bf16 v[88:91], v[176:179], v[104:107], v[88:91]
	v_add_f32_e32 v220, v220, v82
	v_mfma_f32_16x16x32_bf16 v[92:95], v[176:179], v[120:123], v[92:95]
	v_add_f32_e32 v221, v221, v86
	ds_read_b128 v[172:175], v209 offset:18432
	s_waitcnt lgkmcnt(6)
	v_mfma_f32_16x16x32_bf16 v[48:51], v[180:183], v[242:245], v[48:51]
	v_add_f32_e32 v220, v220, v83
	v_mfma_f32_16x16x32_bf16 v[52:55], v[180:183], v[204:207], v[52:55]
	v_add_f32_e32 v221, v221, v87
	ds_read_b128 v[176:179], v203 offset:32768
	s_waitcnt lgkmcnt(6)
	v_mfma_f32_16x16x32_bf16 v[92:95], v[230:233], v[124:127], v[92:95]
	v_cvt_pk_bf16_f32 v218, v72, v73
	v_mfma_f32_16x16x32_bf16 v[88:91], v[230:233], v[108:111], v[88:91]
	v_cvt_pk_bf16_f32 v219, v74, v75
	ds_read_b128 v[180:183], v209 offset:20480
	s_waitcnt lgkmcnt(6)
	v_mfma_f32_16x16x32_bf16 v[60:63], v[234:237], v[204:207], v[60:63]
	v_cvt_pk_bf16_f32 v240, v76, v77
	v_mfma_f32_16x16x32_bf16 v[56:59], v[234:237], v[242:245], v[56:59]
	v_cvt_pk_bf16_f32 v241, v78, v79
	ds_read_b128 v[230:233], v246 offset:32768
	s_waitcnt lgkmcnt(7)
	s_barrier
	s_waitcnt lgkmcnt(6)
	v_mfma_f32_16x16x32_bf16 v[64:67], v[160:163], v[96:99], 0
	v_exp_f32_e32 v88, v88
	v_exp_f32_e32 v92, v92
	v_mfma_f32_16x16x32_bf16 v[68:71], v[160:163], v[112:115], 0
	v_cvt_pk_bf16_f32 v242, v80, v81
	v_exp_f32_e32 v89, v89
	ds_read_b128 v[234:237], v209 offset:22528
	s_add_u32 s8, s16, 0x3bc00280
	s_addc_u32 s9, s17, 0
	s_add_u32 s6, s15, 0x23a60000
	s_addc_u32 s7, s14, 0
	s_waitcnt lgkmcnt(6)
	v_mfma_f32_16x16x32_bf16 v[0:3], v[164:167], v[216:219], v[0:3]
	v_exp_f32_e32 v93, v93
	v_cvt_pk_bf16_f32 v243, v82, v83
	v_mfma_f32_16x16x32_bf16 v[4:7], v[164:167], v[238:241], v[4:7]
	v_exp_f32_e32 v90, v90
	v_exp_f32_e32 v94, v94
	ds_read_b128 v[160:163], v201 offset:36864
	s_waitcnt vmcnt(4)
	ds_write_b128 v225, v[136:139] offset:0
	s_waitcnt lgkmcnt(7)
	v_mfma_f32_16x16x32_bf16 v[68:71], v[168:171], v[116:119], v[68:71]
	v_cvt_pk_bf16_f32 v204, v84, v85
	v_mfma_f32_16x16x32_bf16 v[64:67], v[168:171], v[100:103], v[64:67]
	v_exp_f32_e32 v91, v91
	ds_read_b128 v[164:167], v209 offset:24576
	ds_write_b128 v226, v[140:143] offset:0
	s_waitcnt lgkmcnt(8)
	v_mfma_f32_16x16x32_bf16 v[12:15], v[172:175], v[238:241], v[12:15]
	v_exp_f32_e32 v95, v95
	v_mfma_f32_16x16x32_bf16 v[8:11], v[172:175], v[216:219], v[8:11]
	v_cvt_pk_bf16_f32 v205, v86, v87
	ds_read_b128 v[168:171], v202 offset:36864
	ds_write_b64 v227, v[148:149] offset:49152
	s_waitcnt lgkmcnt(9)
	v_mfma_f32_16x16x32_bf16 v[64:67], v[176:179], v[104:107], v[64:67]
	v_add_f32_e32 v220, v220, v88
	v_mfma_f32_16x16x32_bf16 v[68:71], v[176:179], v[120:123], v[68:71]
	v_add_f32_e32 v221, v221, v92
	ds_read_b128 v[172:175], v209 offset:26624
	ds_write_b64 v228, v[150:151] offset:49152
	s_waitcnt lgkmcnt(10)
	v_mfma_f32_16x16x32_bf16 v[16:19], v[180:183], v[216:219], v[16:19]
	v_add_f32_e32 v220, v220, v89
	v_mfma_f32_16x16x32_bf16 v[20:23], v[180:183], v[238:241], v[20:23]
	v_add_f32_e32 v221, v221, v93
	ds_read_b128 v[176:179], v203 offset:36864
	ds_write_b64 v229, v[144:145] offset:49152
	s_waitcnt lgkmcnt(11)
	v_mfma_f32_16x16x32_bf16 v[68:71], v[230:233], v[124:127], v[68:71]
	v_cvt_pk_bf16_f32 v244, v88, v89
	v_mfma_f32_16x16x32_bf16 v[64:67], v[230:233], v[108:111], v[64:67]
	v_cvt_pk_bf16_f32 v245, v90, v91
	ds_read_b128 v[180:183], v209 offset:28672
	ds_write_b64 v184, v[146:147] offset:49152
	s_waitcnt lgkmcnt(12)
	v_mfma_f32_16x16x32_bf16 v[28:31], v[234:237], v[238:241], v[28:31]
	v_cvt_pk_bf16_f32 v206, v92, v93
	v_mfma_f32_16x16x32_bf16 v[24:27], v[234:237], v[216:219], v[24:27]
	v_cvt_pk_bf16_f32 v207, v94, v95
	ds_read_b128 v[230:233], v246 offset:36864
	global_load_dwordx4 v[148:151], v198, s[8:9]
	s_waitcnt lgkmcnt(12)
	v_mfma_f32_16x16x32_bf16 v[72:75], v[160:163], v[96:99], 0
	v_add_f32_e32 v220, v220, v90
	v_add_f32_e32 v221, v221, v94
	v_mfma_f32_16x16x32_bf16 v[76:79], v[160:163], v[112:115], 0
	v_add_f32_e32 v220, v220, v91
	v_add_f32_e32 v221, v221, v95
	ds_read_b128 v[234:237], v209 offset:30720
	global_load_dwordx4 v[144:147], v199, s[8:9]
	s_waitcnt lgkmcnt(11)
	v_mfma_f32_16x16x32_bf16 v[32:35], v[164:167], v[216:219], v[32:35]
	v_add_f32_e32 v194, v194, v220
	v_add_f32_e32 v195, v195, v221
	v_mfma_f32_16x16x32_bf16 v[36:39], v[164:167], v[238:241], v[36:39]
	v_exp_f32_e32 v64, v64
	v_exp_f32_e32 v68, v68
	ds_read_b128 v[160:163], v201 offset:40960
	global_load_dwordx4 v[136:139], v196, s[6:7]
	s_waitcnt lgkmcnt(10)
	v_mfma_f32_16x16x32_bf16 v[76:79], v[168:171], v[116:119], v[76:79]
	v_exp_f32_e32 v65, v65
	v_mfma_f32_16x16x32_bf16 v[72:75], v[168:171], v[100:103], v[72:75]
	v_exp_f32_e32 v69, v69
	ds_read_b128 v[164:167], v210 offset:16384
	global_load_dwordx4 v[140:143], v197, s[6:7]
	s_waitcnt lgkmcnt(9)
	v_mfma_f32_16x16x32_bf16 v[44:47], v[172:175], v[238:241], v[44:47]
	v_exp_f32_e32 v66, v66
	v_mfma_f32_16x16x32_bf16 v[40:43], v[172:175], v[216:219], v[40:43]
	v_exp_f32_e32 v70, v70
	ds_read_b128 v[168:171], v202 offset:40960
	s_waitcnt lgkmcnt(8)
	v_mfma_f32_16x16x32_bf16 v[72:75], v[176:179], v[104:107], v[72:75]
	v_exp_f32_e32 v67, v67
	v_mfma_f32_16x16x32_bf16 v[76:79], v[176:179], v[120:123], v[76:79]
	v_exp_f32_e32 v71, v71
	ds_read_b128 v[172:175], v210 offset:18432
	s_waitcnt lgkmcnt(7)
	v_mfma_f32_16x16x32_bf16 v[48:51], v[180:183], v[216:219], v[48:51]
	v_add_f32_e32 v220, v64, v65
	v_mfma_f32_16x16x32_bf16 v[52:55], v[180:183], v[238:241], v[52:55]
	v_add_f32_e32 v221, v68, v69
	ds_read_b128 v[176:179], v203 offset:40960
	s_waitcnt lgkmcnt(6)
	v_mfma_f32_16x16x32_bf16 v[76:79], v[230:233], v[124:127], v[76:79]
	v_add_f32_e32 v220, v220, v66
	v_mfma_f32_16x16x32_bf16 v[72:75], v[230:233], v[108:111], v[72:75]
	v_add_f32_e32 v221, v221, v70
	ds_read_b128 v[180:183], v210 offset:20480
	s_waitcnt lgkmcnt(6)
	v_mfma_f32_16x16x32_bf16 v[60:63], v[234:237], v[238:241], v[60:63]
	v_add_f32_e32 v220, v220, v67
	v_mfma_f32_16x16x32_bf16 v[56:59], v[234:237], v[216:219], v[56:59]
	v_add_f32_e32 v221, v221, v71
	ds_read_b128 v[230:233], v246 offset:40960
	s_waitcnt lgkmcnt(6)
	v_mfma_f32_16x16x32_bf16 v[80:83], v[160:163], v[96:99], 0
	v_exp_f32_e32 v72, v72
	v_exp_f32_e32 v76, v76
	v_mfma_f32_16x16x32_bf16 v[84:87], v[160:163], v[112:115], 0
	v_exp_f32_e32 v73, v73
	v_exp_f32_e32 v77, v77
	ds_read_b128 v[234:237], v210 offset:22528
	s_waitcnt lgkmcnt(6)
	v_mfma_f32_16x16x32_bf16 v[0:3], v[164:167], v[242:245], v[0:3]
	v_exp_f32_e32 v74, v74
	v_exp_f32_e32 v78, v78
	v_mfma_f32_16x16x32_bf16 v[4:7], v[164:167], v[204:207], v[4:7]
	v_exp_f32_e32 v75, v75
	v_exp_f32_e32 v79, v79
	ds_read_b128 v[160:163], v201 offset:45056
	s_waitcnt lgkmcnt(6)
	v_mfma_f32_16x16x32_bf16 v[84:87], v[168:171], v[116:119], v[84:87]
	v_add_f32_e32 v220, v220, v72
	v_mfma_f32_16x16x32_bf16 v[80:83], v[168:171], v[100:103], v[80:83]
	v_add_f32_e32 v221, v221, v76
	ds_read_b128 v[164:167], v210 offset:24576
	s_waitcnt lgkmcnt(6)
	v_mfma_f32_16x16x32_bf16 v[12:15], v[172:175], v[204:207], v[12:15]
	v_add_f32_e32 v220, v220, v73
	v_mfma_f32_16x16x32_bf16 v[8:11], v[172:175], v[242:245], v[8:11]
	v_add_f32_e32 v221, v221, v77
	ds_read_b128 v[168:171], v202 offset:45056
	s_waitcnt lgkmcnt(6)
	v_mfma_f32_16x16x32_bf16 v[80:83], v[176:179], v[104:107], v[80:83]
	v_add_f32_e32 v220, v220, v74
	v_mfma_f32_16x16x32_bf16 v[84:87], v[176:179], v[120:123], v[84:87]
	v_add_f32_e32 v221, v221, v78
	ds_read_b128 v[172:175], v210 offset:26624
	s_waitcnt lgkmcnt(6)
	v_mfma_f32_16x16x32_bf16 v[16:19], v[180:183], v[242:245], v[16:19]
	v_add_f32_e32 v220, v220, v75
	v_mfma_f32_16x16x32_bf16 v[20:23], v[180:183], v[204:207], v[20:23]
	v_add_f32_e32 v221, v221, v79
	ds_read_b128 v[176:179], v203 offset:45056
	s_waitcnt lgkmcnt(6)
	v_mfma_f32_16x16x32_bf16 v[84:87], v[230:233], v[124:127], v[84:87]
	v_cvt_pk_bf16_f32 v216, v64, v65
	v_mfma_f32_16x16x32_bf16 v[80:83], v[230:233], v[108:111], v[80:83]
	v_cvt_pk_bf16_f32 v217, v66, v67
	ds_read_b128 v[180:183], v210 offset:28672
	s_waitcnt lgkmcnt(6)
	v_mfma_f32_16x16x32_bf16 v[28:31], v[234:237], v[204:207], v[28:31]
	v_cvt_pk_bf16_f32 v238, v68, v69
	v_mfma_f32_16x16x32_bf16 v[24:27], v[234:237], v[242:245], v[24:27]
	v_cvt_pk_bf16_f32 v239, v70, v71
	ds_read_b128 v[230:233], v246 offset:45056
	s_waitcnt lgkmcnt(6)
	v_mfma_f32_16x16x32_bf16 v[88:91], v[160:163], v[96:99], 0
	v_exp_f32_e32 v80, v80
	v_exp_f32_e32 v84, v84
	v_mfma_f32_16x16x32_bf16 v[92:95], v[160:163], v[112:115], 0
	v_exp_f32_e32 v81, v81
	v_exp_f32_e32 v85, v85
	ds_read_b128 v[234:237], v210 offset:30720
	s_waitcnt lgkmcnt(6)
	v_mfma_f32_16x16x32_bf16 v[32:35], v[164:167], v[242:245], v[32:35]
	v_exp_f32_e32 v82, v82
	v_exp_f32_e32 v86, v86
	v_mfma_f32_16x16x32_bf16 v[36:39], v[164:167], v[204:207], v[36:39]
	v_exp_f32_e32 v83, v83
	v_exp_f32_e32 v87, v87
	ds_read_b128 v[160:163], v201 offset:49152
	s_waitcnt lgkmcnt(6)
	v_mfma_f32_16x16x32_bf16 v[92:95], v[168:171], v[116:119], v[92:95]
	v_add_f32_e32 v220, v220, v80
	v_mfma_f32_16x16x32_bf16 v[88:91], v[168:171], v[100:103], v[88:91]
	v_add_f32_e32 v221, v221, v84
	ds_read_b128 v[164:167], v209 offset:32768
	s_waitcnt lgkmcnt(6)
	v_mfma_f32_16x16x32_bf16 v[44:47], v[172:175], v[204:207], v[44:47]
	v_add_f32_e32 v220, v220, v81
	v_mfma_f32_16x16x32_bf16 v[40:43], v[172:175], v[242:245], v[40:43]
	v_add_f32_e32 v221, v221, v85
	ds_read_b128 v[168:171], v202 offset:49152
	s_waitcnt lgkmcnt(6)
	v_mfma_f32_16x16x32_bf16 v[88:91], v[176:179], v[104:107], v[88:91]
	v_add_f32_e32 v220, v220, v82
	v_mfma_f32_16x16x32_bf16 v[92:95], v[176:179], v[120:123], v[92:95]
	v_add_f32_e32 v221, v221, v86
	ds_read_b128 v[172:175], v209 offset:34816
	s_waitcnt lgkmcnt(6)
	v_mfma_f32_16x16x32_bf16 v[48:51], v[180:183], v[242:245], v[48:51]
	v_add_f32_e32 v220, v220, v83
	v_mfma_f32_16x16x32_bf16 v[52:55], v[180:183], v[204:207], v[52:55]
	v_add_f32_e32 v221, v221, v87
	ds_read_b128 v[176:179], v203 offset:49152
	s_waitcnt lgkmcnt(6)
	v_mfma_f32_16x16x32_bf16 v[92:95], v[230:233], v[124:127], v[92:95]
	v_cvt_pk_bf16_f32 v218, v72, v73
	v_mfma_f32_16x16x32_bf16 v[88:91], v[230:233], v[108:111], v[88:91]
	v_cvt_pk_bf16_f32 v219, v74, v75
	ds_read_b128 v[180:183], v209 offset:36864
	s_waitcnt lgkmcnt(6)
	v_mfma_f32_16x16x32_bf16 v[60:63], v[234:237], v[204:207], v[60:63]
	v_cvt_pk_bf16_f32 v240, v76, v77
	v_mfma_f32_16x16x32_bf16 v[56:59], v[234:237], v[242:245], v[56:59]
	v_cvt_pk_bf16_f32 v241, v78, v79
	ds_read_b128 v[230:233], v246 offset:49152
	s_waitcnt lgkmcnt(7)
	s_barrier
	s_waitcnt lgkmcnt(6)
	v_mfma_f32_16x16x32_bf16 v[64:67], v[160:163], v[96:99], 0
	v_exp_f32_e32 v88, v88
	v_exp_f32_e32 v92, v92
	v_mfma_f32_16x16x32_bf16 v[68:71], v[160:163], v[112:115], 0
	v_cvt_pk_bf16_f32 v242, v80, v81
	v_exp_f32_e32 v89, v89
	ds_read_b128 v[234:237], v209 offset:38912
	s_add_u32 s8, s16, 0x3bc00300
	s_addc_u32 s9, s17, 0
	s_add_u32 s6, s15, 0x23a70000
	s_addc_u32 s7, s14, 0
	s_waitcnt lgkmcnt(6)
	v_mfma_f32_16x16x32_bf16 v[0:3], v[164:167], v[216:219], v[0:3]
	v_exp_f32_e32 v93, v93
	v_cvt_pk_bf16_f32 v243, v82, v83
	v_mfma_f32_16x16x32_bf16 v[4:7], v[164:167], v[238:241], v[4:7]
	v_exp_f32_e32 v90, v90
	v_exp_f32_e32 v94, v94
	ds_read_b128 v[160:163], v201 offset:53248
	s_waitcnt vmcnt(4)
	ds_write_b128 v225, v[152:155] offset:16384
	s_waitcnt lgkmcnt(7)
	v_mfma_f32_16x16x32_bf16 v[68:71], v[168:171], v[116:119], v[68:71]
	v_cvt_pk_bf16_f32 v204, v84, v85
	v_mfma_f32_16x16x32_bf16 v[64:67], v[168:171], v[100:103], v[64:67]
	v_exp_f32_e32 v91, v91
	ds_read_b128 v[164:167], v209 offset:40960
	ds_write_b128 v226, v[156:159] offset:16384
	s_waitcnt lgkmcnt(8)
	v_mfma_f32_16x16x32_bf16 v[12:15], v[172:175], v[238:241], v[12:15]
	v_exp_f32_e32 v95, v95
	v_mfma_f32_16x16x32_bf16 v[8:11], v[172:175], v[216:219], v[8:11]
	v_cvt_pk_bf16_f32 v205, v86, v87
	ds_read_b128 v[168:171], v202 offset:53248
	ds_write_b64 v227, v[132:133] offset:0
	s_waitcnt lgkmcnt(9)
	v_mfma_f32_16x16x32_bf16 v[64:67], v[176:179], v[104:107], v[64:67]
	v_add_f32_e32 v220, v220, v88
	v_mfma_f32_16x16x32_bf16 v[68:71], v[176:179], v[120:123], v[68:71]
	v_add_f32_e32 v221, v221, v92
	ds_read_b128 v[172:175], v209 offset:43008
	ds_write_b64 v228, v[134:135] offset:0
	s_waitcnt lgkmcnt(10)
	v_mfma_f32_16x16x32_bf16 v[16:19], v[180:183], v[216:219], v[16:19]
	v_add_f32_e32 v220, v220, v89
	v_mfma_f32_16x16x32_bf16 v[20:23], v[180:183], v[238:241], v[20:23]
	v_add_f32_e32 v221, v221, v93
	ds_read_b128 v[176:179], v203 offset:53248
	ds_write_b64 v229, v[128:129] offset:0
	s_waitcnt lgkmcnt(11)
	v_mfma_f32_16x16x32_bf16 v[68:71], v[230:233], v[124:127], v[68:71]
	v_cvt_pk_bf16_f32 v244, v88, v89
	v_mfma_f32_16x16x32_bf16 v[64:67], v[230:233], v[108:111], v[64:67]
	v_cvt_pk_bf16_f32 v245, v90, v91
	ds_read_b128 v[180:183], v209 offset:45056
	ds_write_b64 v184, v[130:131] offset:0
	s_waitcnt lgkmcnt(12)
	v_mfma_f32_16x16x32_bf16 v[28:31], v[234:237], v[238:241], v[28:31]
	v_cvt_pk_bf16_f32 v206, v92, v93
	v_mfma_f32_16x16x32_bf16 v[24:27], v[234:237], v[216:219], v[24:27]
	v_cvt_pk_bf16_f32 v207, v94, v95
	ds_read_b128 v[230:233], v246 offset:53248
	global_load_dwordx4 v[132:135], v198, s[8:9]
	s_waitcnt lgkmcnt(12)
	v_mfma_f32_16x16x32_bf16 v[72:75], v[160:163], v[96:99], 0
	v_add_f32_e32 v220, v220, v90
	v_add_f32_e32 v221, v221, v94
	v_mfma_f32_16x16x32_bf16 v[76:79], v[160:163], v[112:115], 0
	v_add_f32_e32 v220, v220, v91
	v_add_f32_e32 v221, v221, v95
	ds_read_b128 v[234:237], v209 offset:47104
	global_load_dwordx4 v[128:131], v199, s[8:9]
	s_waitcnt lgkmcnt(11)
	v_mfma_f32_16x16x32_bf16 v[32:35], v[164:167], v[216:219], v[32:35]
	v_add_f32_e32 v194, v194, v220
	v_add_f32_e32 v195, v195, v221
	v_mfma_f32_16x16x32_bf16 v[36:39], v[164:167], v[238:241], v[36:39]
	v_exp_f32_e32 v64, v64
	v_exp_f32_e32 v68, v68
	ds_read_b128 v[160:163], v201 offset:57344
	global_load_dwordx4 v[152:155], v196, s[6:7]
	s_waitcnt lgkmcnt(10)
	v_mfma_f32_16x16x32_bf16 v[76:79], v[168:171], v[116:119], v[76:79]
	v_exp_f32_e32 v65, v65
	v_mfma_f32_16x16x32_bf16 v[72:75], v[168:171], v[100:103], v[72:75]
	v_exp_f32_e32 v69, v69
	ds_read_b128 v[164:167], v210 offset:32768
	global_load_dwordx4 v[156:159], v197, s[6:7]
	s_waitcnt lgkmcnt(9)
	v_mfma_f32_16x16x32_bf16 v[44:47], v[172:175], v[238:241], v[44:47]
	v_exp_f32_e32 v66, v66
	v_mfma_f32_16x16x32_bf16 v[40:43], v[172:175], v[216:219], v[40:43]
	v_exp_f32_e32 v70, v70
	ds_read_b128 v[168:171], v202 offset:57344
	s_waitcnt lgkmcnt(8)
	v_mfma_f32_16x16x32_bf16 v[72:75], v[176:179], v[104:107], v[72:75]
	v_exp_f32_e32 v67, v67
	v_mfma_f32_16x16x32_bf16 v[76:79], v[176:179], v[120:123], v[76:79]
	v_exp_f32_e32 v71, v71
	ds_read_b128 v[172:175], v210 offset:34816
	s_waitcnt lgkmcnt(7)
	v_mfma_f32_16x16x32_bf16 v[48:51], v[180:183], v[216:219], v[48:51]
	v_add_f32_e32 v220, v64, v65
	v_mfma_f32_16x16x32_bf16 v[52:55], v[180:183], v[238:241], v[52:55]
	v_add_f32_e32 v221, v68, v69
	ds_read_b128 v[176:179], v203 offset:57344
	s_waitcnt lgkmcnt(6)
	v_mfma_f32_16x16x32_bf16 v[76:79], v[230:233], v[124:127], v[76:79]
	v_add_f32_e32 v220, v220, v66
	v_mfma_f32_16x16x32_bf16 v[72:75], v[230:233], v[108:111], v[72:75]
	v_add_f32_e32 v221, v221, v70
	ds_read_b128 v[180:183], v210 offset:36864
	s_waitcnt lgkmcnt(6)
	v_mfma_f32_16x16x32_bf16 v[60:63], v[234:237], v[238:241], v[60:63]
	v_add_f32_e32 v220, v220, v67
	v_mfma_f32_16x16x32_bf16 v[56:59], v[234:237], v[216:219], v[56:59]
	v_add_f32_e32 v221, v221, v71
	ds_read_b128 v[230:233], v246 offset:57344
	s_waitcnt lgkmcnt(6)
	v_mfma_f32_16x16x32_bf16 v[80:83], v[160:163], v[96:99], 0
	v_exp_f32_e32 v72, v72
	v_exp_f32_e32 v76, v76
	v_mfma_f32_16x16x32_bf16 v[84:87], v[160:163], v[112:115], 0
	v_exp_f32_e32 v73, v73
	v_exp_f32_e32 v77, v77
	ds_read_b128 v[234:237], v210 offset:38912
	s_waitcnt lgkmcnt(6)
	v_mfma_f32_16x16x32_bf16 v[0:3], v[164:167], v[242:245], v[0:3]
	v_exp_f32_e32 v74, v74
	v_exp_f32_e32 v78, v78
	v_mfma_f32_16x16x32_bf16 v[4:7], v[164:167], v[204:207], v[4:7]
	v_exp_f32_e32 v75, v75
	v_exp_f32_e32 v79, v79
	ds_read_b128 v[160:163], v201 offset:61440
	s_waitcnt lgkmcnt(6)
	v_mfma_f32_16x16x32_bf16 v[84:87], v[168:171], v[116:119], v[84:87]
	v_add_f32_e32 v220, v220, v72
	v_mfma_f32_16x16x32_bf16 v[80:83], v[168:171], v[100:103], v[80:83]
	v_add_f32_e32 v221, v221, v76
	ds_read_b128 v[164:167], v210 offset:40960
	s_waitcnt lgkmcnt(6)
	v_mfma_f32_16x16x32_bf16 v[12:15], v[172:175], v[204:207], v[12:15]
	v_add_f32_e32 v220, v220, v73
	v_mfma_f32_16x16x32_bf16 v[8:11], v[172:175], v[242:245], v[8:11]
	v_add_f32_e32 v221, v221, v77
	ds_read_b128 v[168:171], v202 offset:61440
	s_waitcnt lgkmcnt(6)
	v_mfma_f32_16x16x32_bf16 v[80:83], v[176:179], v[104:107], v[80:83]
	v_add_f32_e32 v220, v220, v74
	v_mfma_f32_16x16x32_bf16 v[84:87], v[176:179], v[120:123], v[84:87]
	v_add_f32_e32 v221, v221, v78
	ds_read_b128 v[172:175], v210 offset:43008
	s_waitcnt lgkmcnt(6)
	v_mfma_f32_16x16x32_bf16 v[16:19], v[180:183], v[242:245], v[16:19]
	v_add_f32_e32 v220, v220, v75
	v_mfma_f32_16x16x32_bf16 v[20:23], v[180:183], v[204:207], v[20:23]
	v_add_f32_e32 v221, v221, v79
	ds_read_b128 v[176:179], v203 offset:61440
	s_waitcnt lgkmcnt(6)
	v_mfma_f32_16x16x32_bf16 v[84:87], v[230:233], v[124:127], v[84:87]
	v_cvt_pk_bf16_f32 v216, v64, v65
	v_mfma_f32_16x16x32_bf16 v[80:83], v[230:233], v[108:111], v[80:83]
	v_cvt_pk_bf16_f32 v217, v66, v67
	ds_read_b128 v[180:183], v210 offset:45056
	s_waitcnt lgkmcnt(6)
	v_mfma_f32_16x16x32_bf16 v[28:31], v[234:237], v[204:207], v[28:31]
	v_cvt_pk_bf16_f32 v238, v68, v69
	v_mfma_f32_16x16x32_bf16 v[24:27], v[234:237], v[242:245], v[24:27]
	v_cvt_pk_bf16_f32 v239, v70, v71
	ds_read_b128 v[230:233], v246 offset:61440
	s_waitcnt lgkmcnt(6)
	v_mfma_f32_16x16x32_bf16 v[88:91], v[160:163], v[96:99], 0
	v_exp_f32_e32 v80, v80
	v_exp_f32_e32 v84, v84
	v_mfma_f32_16x16x32_bf16 v[92:95], v[160:163], v[112:115], 0
	v_exp_f32_e32 v81, v81
	v_exp_f32_e32 v85, v85
	ds_read_b128 v[234:237], v210 offset:47104
	s_waitcnt lgkmcnt(6)
	v_mfma_f32_16x16x32_bf16 v[32:35], v[164:167], v[242:245], v[32:35]
	v_exp_f32_e32 v82, v82
	v_exp_f32_e32 v86, v86
	v_mfma_f32_16x16x32_bf16 v[36:39], v[164:167], v[204:207], v[36:39]
	v_exp_f32_e32 v83, v83
	v_exp_f32_e32 v87, v87
	ds_read_b128 v[160:163], v201 offset:0
	s_waitcnt lgkmcnt(6)
	v_mfma_f32_16x16x32_bf16 v[92:95], v[168:171], v[116:119], v[92:95]
	v_add_f32_e32 v220, v220, v80
	v_mfma_f32_16x16x32_bf16 v[88:91], v[168:171], v[100:103], v[88:91]
	v_add_f32_e32 v221, v221, v84
	ds_read_b128 v[164:167], v209 offset:49152
	s_waitcnt lgkmcnt(6)
	v_mfma_f32_16x16x32_bf16 v[44:47], v[172:175], v[204:207], v[44:47]
	v_add_f32_e32 v220, v220, v81
	v_mfma_f32_16x16x32_bf16 v[40:43], v[172:175], v[242:245], v[40:43]
	v_add_f32_e32 v221, v221, v85
	ds_read_b128 v[168:171], v202 offset:0
	s_waitcnt lgkmcnt(6)
	v_mfma_f32_16x16x32_bf16 v[88:91], v[176:179], v[104:107], v[88:91]
	v_add_f32_e32 v220, v220, v82
	v_mfma_f32_16x16x32_bf16 v[92:95], v[176:179], v[120:123], v[92:95]
	v_add_f32_e32 v221, v221, v86
	ds_read_b128 v[172:175], v209 offset:51200
	s_waitcnt lgkmcnt(6)
	v_mfma_f32_16x16x32_bf16 v[48:51], v[180:183], v[242:245], v[48:51]
	v_add_f32_e32 v220, v220, v83
	v_mfma_f32_16x16x32_bf16 v[52:55], v[180:183], v[204:207], v[52:55]
	v_add_f32_e32 v221, v221, v87
	ds_read_b128 v[176:179], v203 offset:0
	s_waitcnt lgkmcnt(6)
	v_mfma_f32_16x16x32_bf16 v[92:95], v[230:233], v[124:127], v[92:95]
	v_cvt_pk_bf16_f32 v218, v72, v73
	v_mfma_f32_16x16x32_bf16 v[88:91], v[230:233], v[108:111], v[88:91]
	v_cvt_pk_bf16_f32 v219, v74, v75
	ds_read_b128 v[180:183], v209 offset:53248
	s_waitcnt lgkmcnt(6)
	v_mfma_f32_16x16x32_bf16 v[60:63], v[234:237], v[204:207], v[60:63]
	v_cvt_pk_bf16_f32 v240, v76, v77
	v_mfma_f32_16x16x32_bf16 v[56:59], v[234:237], v[242:245], v[56:59]
	v_cvt_pk_bf16_f32 v241, v78, v79
	ds_read_b128 v[230:233], v246 offset:0
	s_waitcnt lgkmcnt(7)
	s_barrier
	s_waitcnt lgkmcnt(6)
	v_mfma_f32_16x16x32_bf16 v[64:67], v[160:163], v[96:99], 0
	v_exp_f32_e32 v88, v88
	v_exp_f32_e32 v92, v92
	v_mfma_f32_16x16x32_bf16 v[68:71], v[160:163], v[112:115], 0
	v_cvt_pk_bf16_f32 v242, v80, v81
	v_exp_f32_e32 v89, v89
	ds_read_b128 v[234:237], v209 offset:55296
	s_add_u32 s8, s16, 0x3bc00380
	s_addc_u32 s9, s17, 0
	s_add_u32 s6, s15, 0x23a80000
	s_addc_u32 s7, s14, 0
	s_waitcnt lgkmcnt(6)
	v_mfma_f32_16x16x32_bf16 v[0:3], v[164:167], v[216:219], v[0:3]
	v_exp_f32_e32 v93, v93
	v_cvt_pk_bf16_f32 v243, v82, v83
	v_mfma_f32_16x16x32_bf16 v[4:7], v[164:167], v[238:241], v[4:7]
	v_exp_f32_e32 v90, v90
	v_exp_f32_e32 v94, v94
	ds_read_b128 v[160:163], v201 offset:4096
	s_waitcnt vmcnt(4)
	ds_write_b128 v225, v[136:139] offset:32768
	s_waitcnt lgkmcnt(7)
	v_mfma_f32_16x16x32_bf16 v[68:71], v[168:171], v[116:119], v[68:71]
	v_cvt_pk_bf16_f32 v204, v84, v85
	v_mfma_f32_16x16x32_bf16 v[64:67], v[168:171], v[100:103], v[64:67]
	v_exp_f32_e32 v91, v91
	ds_read_b128 v[164:167], v209 offset:57344
	ds_write_b128 v226, v[140:143] offset:32768
	s_waitcnt lgkmcnt(8)
	v_mfma_f32_16x16x32_bf16 v[12:15], v[172:175], v[238:241], v[12:15]
	v_exp_f32_e32 v95, v95
	v_mfma_f32_16x16x32_bf16 v[8:11], v[172:175], v[216:219], v[8:11]
	v_cvt_pk_bf16_f32 v205, v86, v87
	ds_read_b128 v[168:171], v202 offset:4096
	ds_write_b64 v227, v[148:149] offset:16384
	s_waitcnt lgkmcnt(9)
	v_mfma_f32_16x16x32_bf16 v[64:67], v[176:179], v[104:107], v[64:67]
	v_add_f32_e32 v220, v220, v88
	v_mfma_f32_16x16x32_bf16 v[68:71], v[176:179], v[120:123], v[68:71]
	v_add_f32_e32 v221, v221, v92
	ds_read_b128 v[172:175], v209 offset:59392
	ds_write_b64 v228, v[150:151] offset:16384
	s_waitcnt lgkmcnt(10)
	v_mfma_f32_16x16x32_bf16 v[16:19], v[180:183], v[216:219], v[16:19]
	v_add_f32_e32 v220, v220, v89
	v_mfma_f32_16x16x32_bf16 v[20:23], v[180:183], v[238:241], v[20:23]
	v_add_f32_e32 v221, v221, v93
	ds_read_b128 v[176:179], v203 offset:4096
	ds_write_b64 v229, v[144:145] offset:16384
	s_waitcnt lgkmcnt(11)
	v_mfma_f32_16x16x32_bf16 v[68:71], v[230:233], v[124:127], v[68:71]
	v_cvt_pk_bf16_f32 v244, v88, v89
	v_mfma_f32_16x16x32_bf16 v[64:67], v[230:233], v[108:111], v[64:67]
	v_cvt_pk_bf16_f32 v245, v90, v91
	ds_read_b128 v[180:183], v209 offset:61440
	ds_write_b64 v184, v[146:147] offset:16384
	s_waitcnt lgkmcnt(12)
	v_mfma_f32_16x16x32_bf16 v[28:31], v[234:237], v[238:241], v[28:31]
	v_cvt_pk_bf16_f32 v206, v92, v93
	v_mfma_f32_16x16x32_bf16 v[24:27], v[234:237], v[216:219], v[24:27]
	v_cvt_pk_bf16_f32 v207, v94, v95
	ds_read_b128 v[230:233], v246 offset:4096
	global_load_dwordx4 v[148:151], v198, s[8:9]
	s_waitcnt lgkmcnt(12)
	v_mfma_f32_16x16x32_bf16 v[72:75], v[160:163], v[96:99], 0
	v_add_f32_e32 v220, v220, v90
	v_add_f32_e32 v221, v221, v94
	v_mfma_f32_16x16x32_bf16 v[76:79], v[160:163], v[112:115], 0
	v_add_f32_e32 v220, v220, v91
	v_add_f32_e32 v221, v221, v95
	ds_read_b128 v[234:237], v209 offset:63488
	global_load_dwordx4 v[144:147], v199, s[8:9]
	s_waitcnt lgkmcnt(11)
	v_mfma_f32_16x16x32_bf16 v[32:35], v[164:167], v[216:219], v[32:35]
	v_add_f32_e32 v194, v194, v220
	v_add_f32_e32 v195, v195, v221
	v_mfma_f32_16x16x32_bf16 v[36:39], v[164:167], v[238:241], v[36:39]
	v_exp_f32_e32 v64, v64
	v_exp_f32_e32 v68, v68
	ds_read_b128 v[160:163], v201 offset:8192
	global_load_dwordx4 v[136:139], v196, s[6:7]
	s_waitcnt lgkmcnt(10)
	v_mfma_f32_16x16x32_bf16 v[76:79], v[168:171], v[116:119], v[76:79]
	v_exp_f32_e32 v65, v65
	v_mfma_f32_16x16x32_bf16 v[72:75], v[168:171], v[100:103], v[72:75]
	v_exp_f32_e32 v69, v69
	ds_read_b128 v[164:167], v210 offset:49152
	global_load_dwordx4 v[140:143], v197, s[6:7]
	s_waitcnt lgkmcnt(9)
	v_mfma_f32_16x16x32_bf16 v[44:47], v[172:175], v[238:241], v[44:47]
	v_exp_f32_e32 v66, v66
	v_mfma_f32_16x16x32_bf16 v[40:43], v[172:175], v[216:219], v[40:43]
	v_exp_f32_e32 v70, v70
	ds_read_b128 v[168:171], v202 offset:8192
	s_waitcnt lgkmcnt(8)
	v_mfma_f32_16x16x32_bf16 v[72:75], v[176:179], v[104:107], v[72:75]
	v_exp_f32_e32 v67, v67
	v_mfma_f32_16x16x32_bf16 v[76:79], v[176:179], v[120:123], v[76:79]
	v_exp_f32_e32 v71, v71
	ds_read_b128 v[172:175], v210 offset:51200
	s_waitcnt lgkmcnt(7)
	v_mfma_f32_16x16x32_bf16 v[48:51], v[180:183], v[216:219], v[48:51]
	v_add_f32_e32 v220, v64, v65
	v_mfma_f32_16x16x32_bf16 v[52:55], v[180:183], v[238:241], v[52:55]
	v_add_f32_e32 v221, v68, v69
	ds_read_b128 v[176:179], v203 offset:8192
	s_waitcnt lgkmcnt(6)
	v_mfma_f32_16x16x32_bf16 v[76:79], v[230:233], v[124:127], v[76:79]
	v_add_f32_e32 v220, v220, v66
	v_mfma_f32_16x16x32_bf16 v[72:75], v[230:233], v[108:111], v[72:75]
	v_add_f32_e32 v221, v221, v70
	ds_read_b128 v[180:183], v210 offset:53248
	s_waitcnt lgkmcnt(6)
	v_mfma_f32_16x16x32_bf16 v[60:63], v[234:237], v[238:241], v[60:63]
	v_add_f32_e32 v220, v220, v67
	v_mfma_f32_16x16x32_bf16 v[56:59], v[234:237], v[216:219], v[56:59]
	v_add_f32_e32 v221, v221, v71
	ds_read_b128 v[230:233], v246 offset:8192
	s_waitcnt lgkmcnt(6)
	v_mfma_f32_16x16x32_bf16 v[80:83], v[160:163], v[96:99], 0
	v_exp_f32_e32 v72, v72
	v_exp_f32_e32 v76, v76
	v_mfma_f32_16x16x32_bf16 v[84:87], v[160:163], v[112:115], 0
	v_exp_f32_e32 v73, v73
	v_exp_f32_e32 v77, v77
	ds_read_b128 v[234:237], v210 offset:55296
	s_waitcnt lgkmcnt(6)
	v_mfma_f32_16x16x32_bf16 v[0:3], v[164:167], v[242:245], v[0:3]
	v_exp_f32_e32 v74, v74
	v_exp_f32_e32 v78, v78
	v_mfma_f32_16x16x32_bf16 v[4:7], v[164:167], v[204:207], v[4:7]
	v_exp_f32_e32 v75, v75
	v_exp_f32_e32 v79, v79
	ds_read_b128 v[160:163], v201 offset:12288
	s_waitcnt lgkmcnt(6)
	v_mfma_f32_16x16x32_bf16 v[84:87], v[168:171], v[116:119], v[84:87]
	v_add_f32_e32 v220, v220, v72
	v_mfma_f32_16x16x32_bf16 v[80:83], v[168:171], v[100:103], v[80:83]
	v_add_f32_e32 v221, v221, v76
	ds_read_b128 v[164:167], v210 offset:57344
	s_waitcnt lgkmcnt(6)
	v_mfma_f32_16x16x32_bf16 v[12:15], v[172:175], v[204:207], v[12:15]
	v_add_f32_e32 v220, v220, v73
	v_mfma_f32_16x16x32_bf16 v[8:11], v[172:175], v[242:245], v[8:11]
	v_add_f32_e32 v221, v221, v77
	ds_read_b128 v[168:171], v202 offset:12288
	s_waitcnt lgkmcnt(6)
	v_mfma_f32_16x16x32_bf16 v[80:83], v[176:179], v[104:107], v[80:83]
	v_add_f32_e32 v220, v220, v74
	v_mfma_f32_16x16x32_bf16 v[84:87], v[176:179], v[120:123], v[84:87]
	v_add_f32_e32 v221, v221, v78
	ds_read_b128 v[172:175], v210 offset:59392
	s_add_u32 s10, s10, 0x200
	s_addc_u32 s11, s11, 0
	s_add_u32 s12, s12, 0x40000
	s_addc_u32 s13, s13, 0
	s_add_i32 s4, s4, 4
	s_cmpk_lt_u32 s4, 0x104
	s_cselect_b64 s[6:7], -1, 0
	s_and_b64 s[6:7], s[0:1], s[6:7]
	s_and_b64 vcc, exec, s[6:7]
	s_waitcnt lgkmcnt(6)
	v_mfma_f32_16x16x32_bf16 v[16:19], v[180:183], v[242:245], v[16:19]
	v_add_f32_e32 v220, v220, v75
	v_mfma_f32_16x16x32_bf16 v[20:23], v[180:183], v[204:207], v[20:23]
	v_add_f32_e32 v221, v221, v79
	ds_read_b128 v[176:179], v203 offset:12288
	s_waitcnt lgkmcnt(6)
	v_mfma_f32_16x16x32_bf16 v[84:87], v[230:233], v[124:127], v[84:87]
	v_cvt_pk_bf16_f32 v216, v64, v65
	v_mfma_f32_16x16x32_bf16 v[80:83], v[230:233], v[108:111], v[80:83]
	v_cvt_pk_bf16_f32 v217, v66, v67
	ds_read_b128 v[180:183], v210 offset:61440
	s_waitcnt lgkmcnt(6)
	v_mfma_f32_16x16x32_bf16 v[28:31], v[234:237], v[204:207], v[28:31]
	v_cvt_pk_bf16_f32 v238, v68, v69
	v_mfma_f32_16x16x32_bf16 v[24:27], v[234:237], v[242:245], v[24:27]
	v_cvt_pk_bf16_f32 v239, v70, v71
	ds_read_b128 v[230:233], v246 offset:12288
	s_waitcnt lgkmcnt(6)
	v_mfma_f32_16x16x32_bf16 v[88:91], v[160:163], v[96:99], 0
	v_exp_f32_e32 v80, v80
	v_exp_f32_e32 v84, v84
	v_mfma_f32_16x16x32_bf16 v[92:95], v[160:163], v[112:115], 0
	v_exp_f32_e32 v81, v81
	v_exp_f32_e32 v85, v85
	ds_read_b128 v[234:237], v210 offset:63488
	s_waitcnt lgkmcnt(6)
	v_mfma_f32_16x16x32_bf16 v[32:35], v[164:167], v[242:245], v[32:35]
	v_exp_f32_e32 v82, v82
	v_exp_f32_e32 v86, v86
	v_mfma_f32_16x16x32_bf16 v[36:39], v[164:167], v[204:207], v[36:39]
	v_exp_f32_e32 v83, v83
	v_exp_f32_e32 v87, v87
	ds_read_b128 v[160:163], v201 offset:16384
	s_waitcnt lgkmcnt(6)
	v_mfma_f32_16x16x32_bf16 v[92:95], v[168:171], v[116:119], v[92:95]
	v_add_f32_e32 v220, v220, v80
	v_mfma_f32_16x16x32_bf16 v[88:91], v[168:171], v[100:103], v[88:91]
	v_add_f32_e32 v221, v221, v84
	ds_read_b128 v[164:167], v209 offset:0
	s_waitcnt lgkmcnt(6)
	v_mfma_f32_16x16x32_bf16 v[44:47], v[172:175], v[204:207], v[44:47]
	v_add_f32_e32 v220, v220, v81
	v_mfma_f32_16x16x32_bf16 v[40:43], v[172:175], v[242:245], v[40:43]
	v_add_f32_e32 v221, v221, v85
	ds_read_b128 v[168:171], v202 offset:16384
	s_waitcnt lgkmcnt(6)
	v_mfma_f32_16x16x32_bf16 v[88:91], v[176:179], v[104:107], v[88:91]
	v_add_f32_e32 v220, v220, v82
	v_mfma_f32_16x16x32_bf16 v[92:95], v[176:179], v[120:123], v[92:95]
	v_add_f32_e32 v221, v221, v86
	ds_read_b128 v[172:175], v209 offset:2048
	s_waitcnt lgkmcnt(6)
	v_mfma_f32_16x16x32_bf16 v[48:51], v[180:183], v[242:245], v[48:51]
	v_add_f32_e32 v220, v220, v83
	v_mfma_f32_16x16x32_bf16 v[52:55], v[180:183], v[204:207], v[52:55]
	v_add_f32_e32 v221, v221, v87
	ds_read_b128 v[176:179], v203 offset:16384
	s_waitcnt lgkmcnt(6)
	v_mfma_f32_16x16x32_bf16 v[92:95], v[230:233], v[124:127], v[92:95]
	v_cvt_pk_bf16_f32 v218, v72, v73
	v_mfma_f32_16x16x32_bf16 v[88:91], v[230:233], v[108:111], v[88:91]
	v_cvt_pk_bf16_f32 v219, v74, v75
	ds_read_b128 v[180:183], v209 offset:4096
	s_waitcnt lgkmcnt(6)
	v_mfma_f32_16x16x32_bf16 v[60:63], v[234:237], v[204:207], v[60:63]
	v_cvt_pk_bf16_f32 v240, v76, v77
	v_mfma_f32_16x16x32_bf16 v[56:59], v[234:237], v[242:245], v[56:59]
	v_cvt_pk_bf16_f32 v241, v78, v79
	ds_read_b128 v[230:233], v246 offset:16384
	s_waitcnt lgkmcnt(7)
	s_barrier
	s_cbranch_vccnz .LBB0_734
	s_waitcnt vmcnt(0)
	s_nop 7
	s_nop 7
	ds_swizzle_b32 v64, v194 offset:swizzle(SWAP,16)
	s_waitcnt lgkmcnt(0)
	v_add_f32_e32 v194, v194, v64
	v_mov_b32_e32 v65, v194
	s_nop 1
	v_permlane32_swap_b32_e32 v194, v65
	v_add_f32_e32 v194, v194, v65
	s_nop 0
	v_rcp_f32_e32 v66, v194
	ds_swizzle_b32 v64, v195 offset:swizzle(SWAP,16)
	s_waitcnt lgkmcnt(0)
	v_add_f32_e32 v195, v195, v64
	v_mov_b32_e32 v65, v195
	s_nop 1
	v_permlane32_swap_b32_e32 v195, v65
	v_add_f32_e32 v195, v195, v65
	s_nop 0
	v_rcp_f32_e32 v67, v195
	v_readlane_b32 s100, v250, 8
	v_mbcnt_lo_u32_b32 v68, -1, 0
	v_mbcnt_hi_u32_b32 v68, -1, v68
	v_and_b32_e32 v69, 15, v68
	v_lshrrev_b32_e32 v70, 4, v68
	s_lshr_b32 s101, s100, 1
	v_add_u32_e32 v69, s101, v69
	v_lshlrev_b32_e32 v69, 12, v69
	v_and_b32_e32 v71, 1, v70
	v_lshlrev_b32_e32 v71, 5, v71
	v_and_b32_e32 v70, 2, v70
	v_lshl_add_u32 v71, v70, 3, v71
	v_add_u32_e32 v70, v69, v71
	v_add_u32_e32 v71, 0x10000, v70
	v_mul_f32_e32 v0, v0, v66
	v_mul_f32_e32 v1, v1, v66
	v_mul_f32_e32 v2, v2, v66
	v_mul_f32_e32 v3, v3, v66
	v_mul_f32_e32 v8, v8, v66
	v_mul_f32_e32 v9, v9, v66
	v_mul_f32_e32 v10, v10, v66
	v_mul_f32_e32 v11, v11, v66
	v_cvt_pk_bf16_f32 v72, v0, v1
	v_cvt_pk_bf16_f32 v73, v2, v3
	v_cvt_pk_bf16_f32 v74, v8, v9
	v_cvt_pk_bf16_f32 v75, v10, v11
	s_nop 1
	v_permlane16_swap_b32_e32 v72, v74
	v_permlane16_swap_b32_e32 v73, v75
	s_nop 1
	global_store_dwordx4 v70, v[72:75], s[58:59] offset:0
	v_mul_f32_e32 v16, v16, v66
	v_mul_f32_e32 v17, v17, v66
	v_mul_f32_e32 v18, v18, v66
	v_mul_f32_e32 v19, v19, v66
	v_mul_f32_e32 v24, v24, v66
	v_mul_f32_e32 v25, v25, v66
	v_mul_f32_e32 v26, v26, v66
	v_mul_f32_e32 v27, v27, v66
	v_cvt_pk_bf16_f32 v76, v16, v17
	v_cvt_pk_bf16_f32 v77, v18, v19
	v_cvt_pk_bf16_f32 v78, v24, v25
	v_cvt_pk_bf16_f32 v79, v26, v27
	s_nop 1
	v_permlane16_swap_b32_e32 v76, v78
	v_permlane16_swap_b32_e32 v77, v79
	s_nop 1
	global_store_dwordx4 v70, v[76:79], s[58:59] offset:64
	v_mul_f32_e32 v32, v32, v66
	v_mul_f32_e32 v33, v33, v66
	v_mul_f32_e32 v34, v34, v66
	v_mul_f32_e32 v35, v35, v66
	v_mul_f32_e32 v40, v40, v66
	v_mul_f32_e32 v41, v41, v66
	v_mul_f32_e32 v42, v42, v66
	v_mul_f32_e32 v43, v43, v66
	v_cvt_pk_bf16_f32 v80, v32, v33
	v_cvt_pk_bf16_f32 v81, v34, v35
	v_cvt_pk_bf16_f32 v82, v40, v41
	v_cvt_pk_bf16_f32 v83, v42, v43
	s_nop 1
	v_permlane16_swap_b32_e32 v80, v82
	v_permlane16_swap_b32_e32 v81, v83
	s_nop 1
	global_store_dwordx4 v70, v[80:83], s[58:59] offset:128
	v_mul_f32_e32 v48, v48, v66
	v_mul_f32_e32 v49, v49, v66
	v_mul_f32_e32 v50, v50, v66
	v_mul_f32_e32 v51, v51, v66
	v_mul_f32_e32 v56, v56, v66
	v_mul_f32_e32 v57, v57, v66
	v_mul_f32_e32 v58, v58, v66
	v_mul_f32_e32 v59, v59, v66
	v_cvt_pk_bf16_f32 v84, v48, v49
	v_cvt_pk_bf16_f32 v85, v50, v51
	v_cvt_pk_bf16_f32 v86, v56, v57
	v_cvt_pk_bf16_f32 v87, v58, v59
	s_nop 1
	v_permlane16_swap_b32_e32 v84, v86
	v_permlane16_swap_b32_e32 v85, v87
	s_nop 1
	global_store_dwordx4 v70, v[84:87], s[58:59] offset:192
	v_mul_f32_e32 v4, v4, v67
	v_mul_f32_e32 v5, v5, v67
	v_mul_f32_e32 v6, v6, v67
	v_mul_f32_e32 v7, v7, v67
	v_mul_f32_e32 v12, v12, v67
	v_mul_f32_e32 v13, v13, v67
	v_mul_f32_e32 v14, v14, v67
	v_mul_f32_e32 v15, v15, v67
	v_cvt_pk_bf16_f32 v88, v4, v5
	v_cvt_pk_bf16_f32 v89, v6, v7
	v_cvt_pk_bf16_f32 v90, v12, v13
	v_cvt_pk_bf16_f32 v91, v14, v15
	s_nop 1
	v_permlane16_swap_b32_e32 v88, v90
	v_permlane16_swap_b32_e32 v89, v91
	s_nop 1
	global_store_dwordx4 v71, v[88:91], s[58:59] offset:0
	v_mul_f32_e32 v20, v20, v67
	v_mul_f32_e32 v21, v21, v67
	v_mul_f32_e32 v22, v22, v67
	v_mul_f32_e32 v23, v23, v67
	v_mul_f32_e32 v28, v28, v67
	v_mul_f32_e32 v29, v29, v67
	v_mul_f32_e32 v30, v30, v67
	v_mul_f32_e32 v31, v31, v67
	v_cvt_pk_bf16_f32 v92, v20, v21
	v_cvt_pk_bf16_f32 v93, v22, v23
	v_cvt_pk_bf16_f32 v94, v28, v29
	v_cvt_pk_bf16_f32 v95, v30, v31
	s_nop 1
	v_permlane16_swap_b32_e32 v92, v94
	v_permlane16_swap_b32_e32 v93, v95
	s_nop 1
	global_store_dwordx4 v71, v[92:95], s[58:59] offset:64
	v_mul_f32_e32 v36, v36, v67
	v_mul_f32_e32 v37, v37, v67
	v_mul_f32_e32 v38, v38, v67
	v_mul_f32_e32 v39, v39, v67
	v_mul_f32_e32 v44, v44, v67
	v_mul_f32_e32 v45, v45, v67
	v_mul_f32_e32 v46, v46, v67
	v_mul_f32_e32 v47, v47, v67
	v_cvt_pk_bf16_f32 v72, v36, v37
	v_cvt_pk_bf16_f32 v73, v38, v39
	v_cvt_pk_bf16_f32 v74, v44, v45
	v_cvt_pk_bf16_f32 v75, v46, v47
	s_nop 1
	v_permlane16_swap_b32_e32 v72, v74
	v_permlane16_swap_b32_e32 v73, v75
	s_nop 1
	global_store_dwordx4 v71, v[72:75], s[58:59] offset:128
	v_mul_f32_e32 v52, v52, v67
	v_mul_f32_e32 v53, v53, v67
	v_mul_f32_e32 v54, v54, v67
	v_mul_f32_e32 v55, v55, v67
	v_mul_f32_e32 v60, v60, v67
	v_mul_f32_e32 v61, v61, v67
	v_mul_f32_e32 v62, v62, v67
	v_mul_f32_e32 v63, v63, v67
	v_cvt_pk_bf16_f32 v76, v52, v53
	v_cvt_pk_bf16_f32 v77, v54, v55
	v_cvt_pk_bf16_f32 v78, v60, v61
	v_cvt_pk_bf16_f32 v79, v62, v63
	s_nop 1
	v_permlane16_swap_b32_e32 v76, v78
	v_permlane16_swap_b32_e32 v77, v79
	s_nop 1
	global_store_dwordx4 v71, v[76:79], s[58:59] offset:192
	s_barrier
